# gather at 6 waves per SIMD (VGPR alloc 80), otherwise as previous best
# speedup vs baseline: 1.0120x; 1.0120x over previous
	.amdhsa_kernel _Z8k_gatherPK15HIP_vector_typeIiLj2EEPKjPKDv8_DF16_S7_PKfPf
		.amdhsa_group_segment_fixed_size 0
		.amdhsa_private_segment_fixed_size 0
		.amdhsa_kernarg_size 48
		.amdhsa_user_sgpr_count 2
		.amdhsa_user_sgpr_dispatch_ptr 0
		.amdhsa_user_sgpr_queue_ptr 0
		.amdhsa_user_sgpr_kernarg_segment_ptr 1
		.amdhsa_user_sgpr_dispatch_id 0
		.amdhsa_user_sgpr_kernarg_preload_length 0
		.amdhsa_user_sgpr_kernarg_preload_offset 0
		.amdhsa_user_sgpr_private_segment_size 0
		.amdhsa_uses_dynamic_stack 0
		.amdhsa_enable_private_segment 0
		.amdhsa_system_sgpr_workgroup_id_x 1
		.amdhsa_system_sgpr_workgroup_id_y 0
		.amdhsa_system_sgpr_workgroup_id_z 0
		.amdhsa_system_sgpr_workgroup_info 0
		.amdhsa_system_vgpr_workitem_id 0
		.amdhsa_next_free_vgpr 80
		.amdhsa_next_free_sgpr 57
		.amdhsa_accum_offset 80
		.amdhsa_reserve_vcc 1
		.amdhsa_float_round_mode_32 0
		.amdhsa_float_round_mode_16_64 0
		.amdhsa_float_denorm_mode_32 3
		.amdhsa_float_denorm_mode_16_64 3
		.amdhsa_dx10_clamp 1
		.amdhsa_ieee_mode 1
		.amdhsa_fp16_overflow 0
		.amdhsa_tg_split 0
		.amdhsa_exception_fp_ieee_invalid_op 0
		.amdhsa_exception_fp_denorm_src 0
		.amdhsa_exception_fp_ieee_div_zero 0
		.amdhsa_exception_fp_ieee_overflow 0
		.amdhsa_exception_fp_ieee_underflow 0
		.amdhsa_exception_fp_ieee_inexact 0
		.amdhsa_exception_int_div_zero 0
	.end_amdhsa_kernel

amdhsa.kernels:
  - .agpr_count:     0
    .args:
      - .actual_access:  read_only
        .address_space:  global
        .offset:         0
        .size:           8
        .value_kind:     global_buffer
      - .actual_access:  read_only
        .address_space:  global
        .offset:         8
        .size:           8
        .value_kind:     global_buffer
      - .actual_access:  read_only
        .address_space:  global
        .offset:         16
        .size:           8
        .value_kind:     global_buffer
      - .actual_access:  write_only
        .address_space:  global
        .offset:         24
        .size:           8
        .value_kind:     global_buffer
      - .actual_access:  write_only
        .address_space:  global
        .offset:         32
        .size:           8
        .value_kind:     global_buffer
      - .actual_access:  read_only
        .address_space:  global
        .offset:         40
        .size:           8
        .value_kind:     global_buffer
      - .actual_access:  read_only
        .address_space:  global
        .offset:         48
        .size:           8
        .value_kind:     global_buffer
      - .actual_access:  write_only
        .address_space:  global
        .offset:         56
        .size:           8
        .value_kind:     global_buffer
      - .actual_access:  read_only
        .address_space:  global
        .offset:         64
        .size:           8
        .value_kind:     global_buffer
    .group_segment_fixed_size: 27200
    .kernarg_segment_align: 8
    .kernarg_segment_size: 72
    .language:       OpenCL C
    .language_version:
      - 2
      - 0
    .max_flat_workgroup_size: 1024
    .name:           _Z6k_partPKiS0_PKfP15HIP_vector_typeIiLj2EEPiS2_S2_PDv8_DF16_S6_
    .private_segment_fixed_size: 0
    .sgpr_count:     30
    .sgpr_spill_count: 0
    .symbol:         _Z6k_partPKiS0_PKfP15HIP_vector_typeIiLj2EEPiS2_S2_PDv8_DF16_S6_.kd
    .uniform_work_group_size: 1
    .uses_dynamic_stack: false
    .vgpr_count:     30
    .vgpr_spill_count: 0
    .wavefront_size: 64
  - .agpr_count:     0
    .args:
      - .actual_access:  read_only
        .address_space:  global
        .offset:         0
        .size:           8
        .value_kind:     global_buffer
      - .actual_access:  read_only
        .address_space:  global
        .offset:         8
        .size:           8
        .value_kind:     global_buffer
      - .actual_access:  write_only
        .address_space:  global
        .offset:         16
        .size:           8
        .value_kind:     global_buffer
      - .actual_access:  write_only
        .address_space:  global
        .offset:         24
        .size:           8
        .value_kind:     global_buffer
      - .actual_access:  read_only
        .address_space:  global
        .offset:         32
        .size:           8
        .value_kind:     global_buffer
      - .actual_access:  read_only
        .address_space:  global
        .offset:         40
        .size:           8
        .value_kind:     global_buffer
      - .actual_access:  read_only
        .address_space:  global
        .offset:         48
        .size:           8
        .value_kind:     global_buffer
      - .actual_access:  write_only
        .address_space:  global
        .offset:         56
        .size:           8
        .value_kind:     global_buffer
      - .actual_access:  write_only
        .address_space:  global
        .offset:         64
        .size:           8
        .value_kind:     global_buffer
    .group_segment_fixed_size: 51200
    .kernarg_segment_align: 8
    .kernarg_segment_size: 72
    .language:       OpenCL C
    .language_version:
      - 2
      - 0
    .max_flat_workgroup_size: 256
    .name:           _Z6k_gemmPKfPKDv8_DF16_PDF16_S4_PK15HIP_vector_typeIiLj2EEPKiPiPS6_Pj
    .private_segment_fixed_size: 0
    .sgpr_count:     44
    .sgpr_spill_count: 0
    .symbol:         _Z6k_gemmPKfPKDv8_DF16_PDF16_S4_PK15HIP_vector_typeIiLj2EEPKiPiPS6_Pj.kd
    .uniform_work_group_size: 1
    .uses_dynamic_stack: false
    .vgpr_count:     166
    .vgpr_spill_count: 0
    .wavefront_size: 64
  - .agpr_count:     0
    .args:
      - .actual_access:  read_only
        .address_space:  global
        .offset:         0
        .size:           8
        .value_kind:     global_buffer
      - .actual_access:  read_only
        .address_space:  global
        .offset:         8
        .size:           8
        .value_kind:     global_buffer
      - .actual_access:  read_only
        .address_space:  global
        .offset:         16
        .size:           8
        .value_kind:     global_buffer
      - .actual_access:  read_only
        .address_space:  global
        .offset:         24
        .size:           8
        .value_kind:     global_buffer
      - .actual_access:  read_only
        .address_space:  global
        .offset:         32
        .size:           8
        .value_kind:     global_buffer
      - .actual_access:  write_only
        .address_space:  global
        .offset:         40
        .size:           8
        .value_kind:     global_buffer
    .group_segment_fixed_size: 0
    .kernarg_segment_align: 8
    .kernarg_segment_size: 48
    .language:       OpenCL C
    .language_version:
      - 2
      - 0
    .max_flat_workgroup_size: 256
    .name:           _Z8k_gatherPK15HIP_vector_typeIiLj2EEPKjPKDv8_DF16_S7_PKfPf
    .private_segment_fixed_size: 0
    .sgpr_count:     63
    .sgpr_spill_count: 0
    .symbol:         _Z8k_gatherPK15HIP_vector_typeIiLj2EEPKjPKDv8_DF16_S7_PKfPf.kd
    .uniform_work_group_size: 1
    .uses_dynamic_stack: false
    .vgpr_count:     80
    .vgpr_spill_count: 0
    .wavefront_size: 64
